# speedup vs baseline: 1.0116x; 1.0116x over previous
.LBB1_7:
	s_and_b64 s[4:5], s[20:21], exec
	s_cselect_b32 s4, s13, s15
	s_cselect_b32 s5, s12, s14
	s_lshr_b32 s6, s3, 11
	s_lshl_b32 s2, s2, 14
	s_and_b32 s2, s2, 0x3c000
	s_lshl_b32 s3, s6, 21
	s_or_b32 s2, s3, s2
	s_add_u32 s7, s5, s2
	s_mov_b32 s3, 0
	s_addc_u32 s8, s4, 0
	s_lshl_b32 s12, s29, 1
	s_lshr_b32 s9, s30, 8
	s_andn2_b64 vcc, exec, s[18:19]
	s_mov_b64 s[4:5], -1
	s_cbranch_vccnz .LBB1_9
	v_and_b32_e32 v20, 15, v0
	s_lshl_b32 s13, s9, 6
	v_or_b32_e32 v2, s13, v20
	s_movk_i32 s15, 0x410
	s_and_b32 s14, s12, 6
	v_mul_lo_u32 v2, v2, s15
	v_add_u32_e32 v34, 0, v2
	s_lshl_b32 s18, s14, 7
	v_and_b32_e32 v22, 48, v0
	s_lshl_b32 s2, s14, 5
	v_add3_u32 v8, v34, s18, v22
	s_add_i32 s2, s2, s9
	ds_read_b128 v[2:5], v8
	s_lshl_b64 s[4:5], s[2:3], 13
	s_add_u32 s4, s7, s4
	s_addc_u32 s5, s8, s5
	v_lshlrev_b32_e32 v24, 6, v20
	v_mov_b32_e32 v25, 0
	v_lshl_add_u64 v[6:7], s[4:5], 0, v[24:25]
	v_mov_b32_e32 v23, v25
	v_lshl_add_u64 v[10:11], v[6:7], 0, v[22:23]
	s_waitcnt lgkmcnt(0)
	global_store_dwordx4 v[10:11], v[2:5], off sc0 sc1
	v_or_b32_e32 v10, 16, v20
	ds_read_b128 v[6:9], v8 offset:64
	v_or_b32_e32 v2, s13, v10
	v_mul_lo_u32 v2, v2, s15
	v_add_u32_e32 v35, 0, v2
	v_add3_u32 v12, v35, s18, v22
	ds_read_b128 v[2:5], v12
	v_lshlrev_b32_e32 v26, 6, v10
	v_mov_b32_e32 v27, v25
	v_lshl_add_u64 v[10:11], s[4:5], 0, v[26:27]
	v_lshl_add_u64 v[14:15], v[10:11], 0, v[22:23]
	s_waitcnt lgkmcnt(0)
	global_store_dwordx4 v[14:15], v[2:5], off sc0 sc1
	v_or_b32_e32 v14, 32, v20
	ds_read_b128 v[10:13], v12 offset:64
	v_or_b32_e32 v2, s13, v14
	v_mul_lo_u32 v2, v2, s15
	v_add_u32_e32 v36, 0, v2
	v_add3_u32 v16, v36, s18, v22
	ds_read_b128 v[2:5], v16
	v_lshlrev_b32_e32 v28, 6, v14
	v_mov_b32_e32 v29, v25
	v_lshl_add_u64 v[14:15], s[4:5], 0, v[28:29]
	v_lshl_add_u64 v[18:19], v[14:15], 0, v[22:23]
	s_waitcnt lgkmcnt(0)
	global_store_dwordx4 v[18:19], v[2:5], off sc0 sc1
	v_or_b32_e32 v18, 48, v20
	ds_read_b128 v[14:17], v16 offset:64
	v_or_b32_e32 v2, s13, v18
	v_mul_lo_u32 v2, v2, s15
	v_add_u32_e32 v37, 0, v2
	v_add3_u32 v20, v37, s18, v22
	ds_read_b128 v[2:5], v20
	v_lshlrev_b32_e32 v30, 6, v18
	v_mov_b32_e32 v31, v25
	v_lshl_add_u64 v[18:19], s[4:5], 0, v[30:31]
	s_add_u32 s4, s4, 0x1000
	v_lshl_add_u64 v[32:33], v[18:19], 0, v[22:23]
	s_addc_u32 s5, s5, 0
	s_waitcnt lgkmcnt(0)
	global_store_dwordx4 v[32:33], v[2:5], off sc0 sc1
	ds_read_b128 v[18:21], v20 offset:64
	s_or_b32 s2, s14, 1
	v_lshl_add_u64 v[2:3], s[4:5], 0, v[24:25]
	v_lshl_add_u64 v[2:3], v[2:3], 0, v[22:23]
	global_store_dwordx4 v[2:3], v[6:9], off sc0 sc1
	v_lshl_add_u64 v[2:3], s[4:5], 0, v[26:27]
	v_lshl_add_u64 v[2:3], v[2:3], 0, v[22:23]
	global_store_dwordx4 v[2:3], v[10:13], off sc0 sc1
	v_lshl_add_u64 v[2:3], s[4:5], 0, v[28:29]
	v_lshl_add_u64 v[2:3], v[2:3], 0, v[22:23]
	global_store_dwordx4 v[2:3], v[14:17], off sc0 sc1
	v_lshl_add_u64 v[2:3], s[4:5], 0, v[30:31]
	s_lshl_b32 s4, s2, 7
	s_lshl_b32 s2, s2, 5
	s_add_i32 s2, s2, s9
	v_lshl_add_u64 v[2:3], v[2:3], 0, v[22:23]
	v_add3_u32 v10, v34, s4, v22
	s_lshl_b64 s[2:3], s[2:3], 13
	s_waitcnt lgkmcnt(0)
	global_store_dwordx4 v[2:3], v[18:21], off sc0 sc1
	ds_read_b128 v[2:5], v10
	s_add_u32 s2, s7, s2
	s_addc_u32 s3, s8, s3
	v_lshl_add_u64 v[6:7], s[2:3], 0, v[24:25]
	v_add3_u32 v16, v35, s4, v22
	v_lshl_add_u64 v[14:15], v[6:7], 0, v[22:23]
	ds_read_b128 v[6:9], v16
	ds_read_b128 v[10:13], v10 offset:64
	s_waitcnt lgkmcnt(2)
	global_store_dwordx4 v[14:15], v[2:5], off sc0 sc1
	v_add3_u32 v18, v36, s4, v22
	v_add3_u32 v34, v37, s4, v22
	v_lshl_add_u64 v[2:3], s[2:3], 0, v[26:27]
	v_lshl_add_u64 v[14:15], v[2:3], 0, v[22:23]
	ds_read_b128 v[2:5], v16 offset:64
	s_waitcnt lgkmcnt(2)
	global_store_dwordx4 v[14:15], v[6:9], off sc0 sc1
	ds_read_b128 v[6:9], v18
	v_lshl_add_u64 v[14:15], s[2:3], 0, v[28:29]
	v_lshl_add_u64 v[32:33], v[14:15], 0, v[22:23]
	ds_read_b128 v[14:17], v34
	ds_read_b128 v[18:21], v18 offset:64
	s_mov_b64 s[4:5], 0
	s_waitcnt lgkmcnt(2)
	global_store_dwordx4 v[32:33], v[6:9], off sc0 sc1
	s_nop 1
	v_lshl_add_u64 v[6:7], s[2:3], 0, v[30:31]
	s_add_u32 s2, s2, 0x1000
	v_lshl_add_u64 v[32:33], v[6:7], 0, v[22:23]
	s_addc_u32 s3, s3, 0
	s_waitcnt lgkmcnt(1)
	global_store_dwordx4 v[32:33], v[14:17], off sc0 sc1
	ds_read_b128 v[6:9], v34 offset:64
	s_nop 0
	v_lshl_add_u64 v[14:15], s[2:3], 0, v[24:25]
	v_lshl_add_u64 v[14:15], v[14:15], 0, v[22:23]
	global_store_dwordx4 v[14:15], v[10:13], off sc0 sc1
	s_nop 1
	v_lshl_add_u64 v[10:11], s[2:3], 0, v[26:27]
	v_lshl_add_u64 v[10:11], v[10:11], 0, v[22:23]
	global_store_dwordx4 v[10:11], v[2:5], off sc0 sc1
	s_nop 1
	v_lshl_add_u64 v[2:3], s[2:3], 0, v[28:29]
	v_lshl_add_u64 v[2:3], v[2:3], 0, v[22:23]
	s_waitcnt lgkmcnt(1)
	global_store_dwordx4 v[2:3], v[18:21], off sc0 sc1
	v_lshl_add_u64 v[2:3], s[2:3], 0, v[30:31]
	v_lshl_add_u64 v[2:3], v[2:3], 0, v[22:23]
	s_waitcnt lgkmcnt(0)
	global_store_dwordx4 v[2:3], v[6:9], off sc0 sc1
.LBB1_9:
	s_andn2_b64 vcc, exec, s[4:5]
	s_cbranch_vccnz .LBB1_13
	v_lshl_or_b32 v2, s9, 6, v1
	s_movk_i32 s13, 0x410
	v_mul_lo_u32 v2, v2, s13
	v_add_u32_e32 v22, 0, v2
	s_and_b32 s12, s12, 6
	v_lshl_add_u32 v23, s12, 7, v22
	s_lshl_b32 s2, s12, 5
	ds_read_b128 v[2:5], v23
	ds_read_b128 v[6:9], v23 offset:16
	ds_read_b128 v[10:13], v23 offset:32
	ds_read_b128 v[14:17], v23 offset:48
	s_mov_b32 s3, 0
	s_add_i32 s2, s2, s9
	s_lshl_b64 s[4:5], s[2:3], 13
	s_add_u32 s4, s7, s4
	s_addc_u32 s5, s8, s5
	v_lshlrev_b32_e32 v18, 4, v1
	s_waitcnt lgkmcnt(3)
	global_store_dwordx4 v18, v[2:5], s[4:5] sc0 sc1
	s_waitcnt lgkmcnt(2)
	global_store_dwordx4 v18, v[6:9], s[4:5] offset:1024 sc0 sc1
	s_waitcnt lgkmcnt(1)
	global_store_dwordx4 v18, v[10:13], s[4:5] offset:2048 sc0 sc1
	s_waitcnt lgkmcnt(0)
	global_store_dwordx4 v18, v[14:17], s[4:5] offset:3072 sc0 sc1
	ds_read_b128 v[2:5], v23 offset:64
	ds_read_b128 v[6:9], v23 offset:80
	ds_read_b128 v[10:13], v23 offset:96
	ds_read_b128 v[14:17], v23 offset:112
	v_mov_b32_e32 v19, 0
	v_lshl_add_u64 v[20:21], s[4:5], 0, v[18:19]
	s_movk_i32 s4, 0x1000
	v_add_co_u32_e32 v20, vcc, s4, v20
	s_or_b32 s2, s12, 1
	s_nop 0
	v_addc_co_u32_e32 v21, vcc, 0, v21, vcc
	s_waitcnt lgkmcnt(3)
	global_store_dwordx4 v[20:21], v[2:5], off sc0 sc1
	s_waitcnt lgkmcnt(2)
	global_store_dwordx4 v[20:21], v[6:9], off offset:1024 sc0 sc1
	s_waitcnt lgkmcnt(1)
	global_store_dwordx4 v[20:21], v[10:13], off offset:2048 sc0 sc1
	s_waitcnt lgkmcnt(0)
	global_store_dwordx4 v[20:21], v[14:17], off offset:3072 sc0 sc1
	v_lshl_add_u32 v22, s2, 7, v22
	s_lshl_b32 s2, s2, 5
	ds_read_b128 v[2:5], v22
	ds_read_b128 v[6:9], v22 offset:16
	ds_read_b128 v[10:13], v22 offset:32
	ds_read_b128 v[14:17], v22 offset:48
	s_add_i32 s2, s2, s9
	s_lshl_b64 s[2:3], s[2:3], 13
	s_add_u32 s2, s7, s2
	s_addc_u32 s3, s8, s3
	s_waitcnt lgkmcnt(3)
	global_store_dwordx4 v18, v[2:5], s[2:3] sc0 sc1
	s_waitcnt lgkmcnt(2)
	global_store_dwordx4 v18, v[6:9], s[2:3] offset:1024 sc0 sc1
	s_waitcnt lgkmcnt(1)
	global_store_dwordx4 v18, v[10:13], s[2:3] offset:2048 sc0 sc1
	s_waitcnt lgkmcnt(0)
	global_store_dwordx4 v18, v[14:17], s[2:3] offset:3072 sc0 sc1
	ds_read_b128 v[2:5], v22 offset:64
	ds_read_b128 v[6:9], v22 offset:80
	ds_read_b128 v[10:13], v22 offset:96
	ds_read_b128 v[14:17], v22 offset:112
	v_lshl_add_u64 v[20:21], s[2:3], 0, v[18:19]
	v_add_co_u32_e32 v18, vcc, s4, v20
	s_nop 1
	v_addc_co_u32_e32 v19, vcc, 0, v21, vcc
	s_waitcnt lgkmcnt(3)
	global_store_dwordx4 v[18:19], v[2:5], off sc0 sc1
	s_waitcnt lgkmcnt(2)
	global_store_dwordx4 v[18:19], v[6:9], off offset:1024 sc0 sc1
	s_waitcnt lgkmcnt(1)
	global_store_dwordx4 v[18:19], v[10:13], off offset:2048 sc0 sc1
	s_waitcnt lgkmcnt(0)
	global_store_dwordx4 v[18:19], v[14:17], off offset:3072 sc0 sc1
	v_and_b32_e32 v2, 7, v0
	v_lshl_add_u32 v18, v2, 7, 0
	v_lshl_add_u32 v6, v2, 2, 0
	v_lshrrev_b32_e32 v2, 3, v0
	v_mad_u32_u24 v19, v2, s13, v18
	ds_read_b128 v[2:5], v19
	v_add_u32_e32 v20, 0x20800, v6
	ds_read_b128 v[6:9], v19 offset:16
	ds_read_b128 v[10:13], v19 offset:32
	ds_read_b128 v[14:17], v19 offset:48
	ds_read_b128 v[28:31], v19 offset:64
	ds_read_b128 v[32:35], v19 offset:80
	ds_read_b128 v[36:39], v19 offset:96
	ds_read_b128 v[40:43], v19 offset:112
	v_or_b32_e32 v21, 0x200, v0
	v_lshrrev_b32_e32 v21, 3, v21
	v_mad_u32_u24 v18, v21, s13, v18
	ds_read_b128 v[44:47], v18
	ds_read_b128 v[48:51], v18 offset:16
	ds_read_b128 v[52:55], v18 offset:32
	ds_read_b128 v[56:59], v18 offset:48
	s_waitcnt lgkmcnt(8)
	v_fma_mix_f32 v24, v2, v2, 0 op_sel_hi:[1,1,0]
	v_fma_mix_f32 v25, v6, v6, 0 op_sel_hi:[1,1,0]
	v_fma_mix_f32 v26, v10, v10, 0 op_sel_hi:[1,1,0]
	v_fma_mix_f32 v27, v14, v14, 0 op_sel_hi:[1,1,0]
	v_fma_mix_f32 v24, v2, v2, v24 op_sel:[1,1,0] op_sel_hi:[1,1,0]
	v_fma_mix_f32 v25, v6, v6, v25 op_sel:[1,1,0] op_sel_hi:[1,1,0]
	v_fma_mix_f32 v26, v10, v10, v26 op_sel:[1,1,0] op_sel_hi:[1,1,0]
	v_fma_mix_f32 v27, v14, v14, v27 op_sel:[1,1,0] op_sel_hi:[1,1,0]
	v_fma_mix_f32 v24, v3, v3, v24 op_sel_hi:[1,1,0]
	v_fma_mix_f32 v25, v7, v7, v25 op_sel_hi:[1,1,0]
	v_fma_mix_f32 v26, v11, v11, v26 op_sel_hi:[1,1,0]
	v_fma_mix_f32 v27, v15, v15, v27 op_sel_hi:[1,1,0]
	v_fma_mix_f32 v24, v3, v3, v24 op_sel:[1,1,0] op_sel_hi:[1,1,0]
	v_fma_mix_f32 v25, v7, v7, v25 op_sel:[1,1,0] op_sel_hi:[1,1,0]
	v_fma_mix_f32 v26, v11, v11, v26 op_sel:[1,1,0] op_sel_hi:[1,1,0]
	v_fma_mix_f32 v27, v15, v15, v27 op_sel:[1,1,0] op_sel_hi:[1,1,0]
	v_fma_mix_f32 v24, v4, v4, v24 op_sel_hi:[1,1,0]
	v_fma_mix_f32 v25, v8, v8, v25 op_sel_hi:[1,1,0]
	v_fma_mix_f32 v26, v12, v12, v26 op_sel_hi:[1,1,0]
	v_fma_mix_f32 v27, v16, v16, v27 op_sel_hi:[1,1,0]
	v_fma_mix_f32 v24, v4, v4, v24 op_sel:[1,1,0] op_sel_hi:[1,1,0]
	v_fma_mix_f32 v25, v8, v8, v25 op_sel:[1,1,0] op_sel_hi:[1,1,0]
	v_fma_mix_f32 v26, v12, v12, v26 op_sel:[1,1,0] op_sel_hi:[1,1,0]
	v_fma_mix_f32 v27, v16, v16, v27 op_sel:[1,1,0] op_sel_hi:[1,1,0]
	v_fma_mix_f32 v24, v5, v5, v24 op_sel_hi:[1,1,0]
	v_fma_mix_f32 v25, v9, v9, v25 op_sel_hi:[1,1,0]
	v_fma_mix_f32 v26, v13, v13, v26 op_sel_hi:[1,1,0]
	v_fma_mix_f32 v27, v17, v17, v27 op_sel_hi:[1,1,0]
	v_fma_mix_f32 v24, v5, v5, v24 op_sel:[1,1,0] op_sel_hi:[1,1,0]
	v_fma_mix_f32 v25, v9, v9, v25 op_sel:[1,1,0] op_sel_hi:[1,1,0]
	v_fma_mix_f32 v26, v13, v13, v26 op_sel:[1,1,0] op_sel_hi:[1,1,0]
	v_fma_mix_f32 v27, v17, v17, v27 op_sel:[1,1,0] op_sel_hi:[1,1,0]
	ds_read_b128 v[60:63], v18 offset:64
	ds_read_b128 v[64:67], v18 offset:80
	ds_read_b128 v[68:71], v18 offset:96
	ds_read_b128 v[72:75], v18 offset:112
	s_waitcnt lgkmcnt(8)
	v_fma_mix_f32 v24, v28, v28, v24 op_sel_hi:[1,1,0]
	v_fma_mix_f32 v25, v32, v32, v25 op_sel_hi:[1,1,0]
	v_fma_mix_f32 v26, v36, v36, v26 op_sel_hi:[1,1,0]
	v_fma_mix_f32 v27, v40, v40, v27 op_sel_hi:[1,1,0]
	v_fma_mix_f32 v24, v28, v28, v24 op_sel:[1,1,0] op_sel_hi:[1,1,0]
	v_fma_mix_f32 v25, v32, v32, v25 op_sel:[1,1,0] op_sel_hi:[1,1,0]
	v_fma_mix_f32 v26, v36, v36, v26 op_sel:[1,1,0] op_sel_hi:[1,1,0]
	v_fma_mix_f32 v27, v40, v40, v27 op_sel:[1,1,0] op_sel_hi:[1,1,0]
	v_fma_mix_f32 v24, v29, v29, v24 op_sel_hi:[1,1,0]
	v_fma_mix_f32 v25, v33, v33, v25 op_sel_hi:[1,1,0]
	v_fma_mix_f32 v26, v37, v37, v26 op_sel_hi:[1,1,0]
	v_fma_mix_f32 v27, v41, v41, v27 op_sel_hi:[1,1,0]
	v_fma_mix_f32 v24, v29, v29, v24 op_sel:[1,1,0] op_sel_hi:[1,1,0]
	v_fma_mix_f32 v25, v33, v33, v25 op_sel:[1,1,0] op_sel_hi:[1,1,0]
	v_fma_mix_f32 v26, v37, v37, v26 op_sel:[1,1,0] op_sel_hi:[1,1,0]
	v_fma_mix_f32 v27, v41, v41, v27 op_sel:[1,1,0] op_sel_hi:[1,1,0]
	v_fma_mix_f32 v24, v30, v30, v24 op_sel_hi:[1,1,0]
	v_fma_mix_f32 v25, v34, v34, v25 op_sel_hi:[1,1,0]
	v_fma_mix_f32 v26, v38, v38, v26 op_sel_hi:[1,1,0]
	v_fma_mix_f32 v27, v42, v42, v27 op_sel_hi:[1,1,0]
	v_fma_mix_f32 v24, v30, v30, v24 op_sel:[1,1,0] op_sel_hi:[1,1,0]
	v_fma_mix_f32 v25, v34, v34, v25 op_sel:[1,1,0] op_sel_hi:[1,1,0]
	v_fma_mix_f32 v26, v38, v38, v26 op_sel:[1,1,0] op_sel_hi:[1,1,0]
	v_fma_mix_f32 v27, v42, v42, v27 op_sel:[1,1,0] op_sel_hi:[1,1,0]
	v_fma_mix_f32 v24, v31, v31, v24 op_sel_hi:[1,1,0]
	v_fma_mix_f32 v25, v35, v35, v25 op_sel_hi:[1,1,0]
	v_fma_mix_f32 v26, v39, v39, v26 op_sel_hi:[1,1,0]
	v_fma_mix_f32 v27, v43, v43, v27 op_sel_hi:[1,1,0]
	v_fma_mix_f32 v24, v31, v31, v24 op_sel:[1,1,0] op_sel_hi:[1,1,0]
	v_fma_mix_f32 v25, v35, v35, v25 op_sel:[1,1,0] op_sel_hi:[1,1,0]
	v_fma_mix_f32 v26, v39, v39, v26 op_sel:[1,1,0] op_sel_hi:[1,1,0]
	v_fma_mix_f32 v27, v43, v43, v27 op_sel:[1,1,0] op_sel_hi:[1,1,0]
	v_add_f32_e32 v24, v24, v25
	v_add_f32_e32 v26, v26, v27
	s_nop 0
	v_add_f32_e32 v24, v24, v26
	s_nop 0
	ds_max_u32 v20, v24
	s_waitcnt lgkmcnt(5)
	v_fma_mix_f32 v24, v44, v44, 0 op_sel_hi:[1,1,0]
	v_fma_mix_f32 v25, v48, v48, 0 op_sel_hi:[1,1,0]
	v_fma_mix_f32 v26, v52, v52, 0 op_sel_hi:[1,1,0]
	v_fma_mix_f32 v27, v56, v56, 0 op_sel_hi:[1,1,0]
	v_fma_mix_f32 v24, v44, v44, v24 op_sel:[1,1,0] op_sel_hi:[1,1,0]
	v_fma_mix_f32 v25, v48, v48, v25 op_sel:[1,1,0] op_sel_hi:[1,1,0]
	v_fma_mix_f32 v26, v52, v52, v26 op_sel:[1,1,0] op_sel_hi:[1,1,0]
	v_fma_mix_f32 v27, v56, v56, v27 op_sel:[1,1,0] op_sel_hi:[1,1,0]
	v_fma_mix_f32 v24, v45, v45, v24 op_sel_hi:[1,1,0]
	v_fma_mix_f32 v25, v49, v49, v25 op_sel_hi:[1,1,0]
	v_fma_mix_f32 v26, v53, v53, v26 op_sel_hi:[1,1,0]
	v_fma_mix_f32 v27, v57, v57, v27 op_sel_hi:[1,1,0]
	v_fma_mix_f32 v24, v45, v45, v24 op_sel:[1,1,0] op_sel_hi:[1,1,0]
	v_fma_mix_f32 v25, v49, v49, v25 op_sel:[1,1,0] op_sel_hi:[1,1,0]
	v_fma_mix_f32 v26, v53, v53, v26 op_sel:[1,1,0] op_sel_hi:[1,1,0]
	v_fma_mix_f32 v27, v57, v57, v27 op_sel:[1,1,0] op_sel_hi:[1,1,0]
	v_fma_mix_f32 v24, v46, v46, v24 op_sel_hi:[1,1,0]
	v_fma_mix_f32 v25, v50, v50, v25 op_sel_hi:[1,1,0]
	v_fma_mix_f32 v26, v54, v54, v26 op_sel_hi:[1,1,0]
	v_fma_mix_f32 v27, v58, v58, v27 op_sel_hi:[1,1,0]
	v_fma_mix_f32 v24, v46, v46, v24 op_sel:[1,1,0] op_sel_hi:[1,1,0]
	v_fma_mix_f32 v25, v50, v50, v25 op_sel:[1,1,0] op_sel_hi:[1,1,0]
	v_fma_mix_f32 v26, v54, v54, v26 op_sel:[1,1,0] op_sel_hi:[1,1,0]
	v_fma_mix_f32 v27, v58, v58, v27 op_sel:[1,1,0] op_sel_hi:[1,1,0]
	v_fma_mix_f32 v24, v47, v47, v24 op_sel_hi:[1,1,0]
	v_fma_mix_f32 v25, v51, v51, v25 op_sel_hi:[1,1,0]
	v_fma_mix_f32 v26, v55, v55, v26 op_sel_hi:[1,1,0]
	v_fma_mix_f32 v27, v59, v59, v27 op_sel_hi:[1,1,0]
	v_fma_mix_f32 v24, v47, v47, v24 op_sel:[1,1,0] op_sel_hi:[1,1,0]
	v_fma_mix_f32 v25, v51, v51, v25 op_sel:[1,1,0] op_sel_hi:[1,1,0]
	v_fma_mix_f32 v26, v55, v55, v26 op_sel:[1,1,0] op_sel_hi:[1,1,0]
	v_fma_mix_f32 v27, v59, v59, v27 op_sel:[1,1,0] op_sel_hi:[1,1,0]
	s_waitcnt lgkmcnt(1)
	v_fma_mix_f32 v24, v60, v60, v24 op_sel_hi:[1,1,0]
	v_fma_mix_f32 v25, v64, v64, v25 op_sel_hi:[1,1,0]
	v_fma_mix_f32 v26, v68, v68, v26 op_sel_hi:[1,1,0]
	v_fma_mix_f32 v27, v72, v72, v27 op_sel_hi:[1,1,0]
	v_fma_mix_f32 v24, v60, v60, v24 op_sel:[1,1,0] op_sel_hi:[1,1,0]
	v_fma_mix_f32 v25, v64, v64, v25 op_sel:[1,1,0] op_sel_hi:[1,1,0]
	v_fma_mix_f32 v26, v68, v68, v26 op_sel:[1,1,0] op_sel_hi:[1,1,0]
	v_fma_mix_f32 v27, v72, v72, v27 op_sel:[1,1,0] op_sel_hi:[1,1,0]
	v_fma_mix_f32 v24, v61, v61, v24 op_sel_hi:[1,1,0]
	v_fma_mix_f32 v25, v65, v65, v25 op_sel_hi:[1,1,0]
	v_fma_mix_f32 v26, v69, v69, v26 op_sel_hi:[1,1,0]
	v_fma_mix_f32 v27, v73, v73, v27 op_sel_hi:[1,1,0]
	v_fma_mix_f32 v24, v61, v61, v24 op_sel:[1,1,0] op_sel_hi:[1,1,0]
	v_fma_mix_f32 v25, v65, v65, v25 op_sel:[1,1,0] op_sel_hi:[1,1,0]
	v_fma_mix_f32 v26, v69, v69, v26 op_sel:[1,1,0] op_sel_hi:[1,1,0]
	v_fma_mix_f32 v27, v73, v73, v27 op_sel:[1,1,0] op_sel_hi:[1,1,0]
	v_fma_mix_f32 v24, v62, v62, v24 op_sel_hi:[1,1,0]
	v_fma_mix_f32 v25, v66, v66, v25 op_sel_hi:[1,1,0]
	v_fma_mix_f32 v26, v70, v70, v26 op_sel_hi:[1,1,0]
	v_fma_mix_f32 v27, v74, v74, v27 op_sel_hi:[1,1,0]
	v_fma_mix_f32 v24, v62, v62, v24 op_sel:[1,1,0] op_sel_hi:[1,1,0]
	v_fma_mix_f32 v25, v66, v66, v25 op_sel:[1,1,0] op_sel_hi:[1,1,0]
	v_fma_mix_f32 v26, v70, v70, v26 op_sel:[1,1,0] op_sel_hi:[1,1,0]
	v_fma_mix_f32 v27, v74, v74, v27 op_sel:[1,1,0] op_sel_hi:[1,1,0]
	v_fma_mix_f32 v24, v63, v63, v24 op_sel_hi:[1,1,0]
	v_fma_mix_f32 v25, v67, v67, v25 op_sel_hi:[1,1,0]
	v_fma_mix_f32 v26, v71, v71, v26 op_sel_hi:[1,1,0]
	v_fma_mix_f32 v27, v75, v75, v27 op_sel_hi:[1,1,0]
	v_fma_mix_f32 v24, v63, v63, v24 op_sel:[1,1,0] op_sel_hi:[1,1,0]
	v_fma_mix_f32 v25, v67, v67, v25 op_sel:[1,1,0] op_sel_hi:[1,1,0]
	v_fma_mix_f32 v26, v71, v71, v26 op_sel:[1,1,0] op_sel_hi:[1,1,0]
	v_fma_mix_f32 v27, v75, v75, v27 op_sel:[1,1,0] op_sel_hi:[1,1,0]
	v_add_f32_e32 v24, v24, v25
	v_add_f32_e32 v26, v26, v27
	s_nop 0
	v_add_f32_e32 v24, v24, v26
	s_nop 0
	ds_max_u32 v20, v24
	s_waitcnt lgkmcnt(0)
	s_barrier
	s_and_saveexec_b64 s[2:3], s[0:1]
	s_cbranch_execz .LBB1_12
	v_lshlrev_b32_e32 v0, 2, v0
	v_add_u32_e32 v2, 0, v0
	v_add_u32_e32 v2, 0x20800, v2
	ds_read_b32 v2, v2
	s_lshl_b32 s0, s6, 5
	s_add_u32 s0, s16, s0
	s_addc_u32 s1, s17, 0
	s_waitcnt lgkmcnt(0)
	global_atomic_umax v0, v2, s[0:1]

.LBB1_14:
	s_lshl_b32 s4, s29, 4
	v_lshlrev_b32_e32 v0, 4, v1
	s_mov_b32 s1, 0
	v_mov_b32_e32 v1, 0
	s_add_i32 s0, s4, s28
	v_lshl_add_u64 v[8:9], s[10:11], 0, v[0:1]
	s_lshl_b64 s[2:3], s[0:1], 10
	v_add_u32_e32 v4, 0, v0
	s_mulk_i32 s29, 0x4100
	v_lshl_add_u64 v[10:11], v[8:9], 0, s[2:3]
	s_or_b32 s2, s4, 1
	v_add_u32_e32 v0, s29, v4
	s_mul_i32 s3, s2, 0x410
	ds_read_b128 v[0:3], v0
	v_add_u32_e32 v12, s3, v4
	ds_read_b128 v[4:7], v12
	s_add_i32 s2, s2, s28
	s_mov_b32 s3, s1
	s_lshl_b64 s[2:3], s[2:3], 10
	s_waitcnt lgkmcnt(1)
	global_store_dwordx4 v[10:11], v[0:3], off sc0 sc1
	s_nop 1
	v_lshl_add_u64 v[0:1], v[8:9], 0, s[2:3]
	s_waitcnt lgkmcnt(0)
	global_store_dwordx4 v[0:1], v[4:7], off sc0 sc1
	ds_read_b128 v[0:3], v12 offset:1040
	ds_read_b128 v[4:7], v12 offset:2080
	s_add_i32 s2, s0, 2
	s_mov_b32 s3, s1
	s_lshl_b64 s[2:3], s[2:3], 10
	v_lshl_add_u64 v[10:11], v[8:9], 0, s[2:3]
	s_add_i32 s2, s0, 3
	s_mov_b32 s3, s1
	s_lshl_b64 s[2:3], s[2:3], 10
	s_waitcnt lgkmcnt(1)
	global_store_dwordx4 v[10:11], v[0:3], off sc0 sc1
	s_nop 1
	v_lshl_add_u64 v[0:1], v[8:9], 0, s[2:3]
	s_waitcnt lgkmcnt(0)
	global_store_dwordx4 v[0:1], v[4:7], off sc0 sc1
	ds_read_b128 v[0:3], v12 offset:3120
	ds_read_b128 v[4:7], v12 offset:4160
	s_add_i32 s2, s0, 4
	s_mov_b32 s3, s1
	s_lshl_b64 s[2:3], s[2:3], 10
	v_lshl_add_u64 v[10:11], v[8:9], 0, s[2:3]
	s_add_i32 s2, s0, 5
	s_mov_b32 s3, s1
	s_lshl_b64 s[2:3], s[2:3], 10
	s_waitcnt lgkmcnt(1)
	global_store_dwordx4 v[10:11], v[0:3], off sc0 sc1
	s_nop 1
	v_lshl_add_u64 v[0:1], v[8:9], 0, s[2:3]
	s_waitcnt lgkmcnt(0)
	global_store_dwordx4 v[0:1], v[4:7], off sc0 sc1
	ds_read_b128 v[0:3], v12 offset:5200
	ds_read_b128 v[4:7], v12 offset:6240
	s_add_i32 s2, s0, 6
	s_mov_b32 s3, s1
	s_lshl_b64 s[2:3], s[2:3], 10
	v_lshl_add_u64 v[10:11], v[8:9], 0, s[2:3]
	s_add_i32 s2, s0, 7
	s_mov_b32 s3, s1
	s_lshl_b64 s[2:3], s[2:3], 10
	s_waitcnt lgkmcnt(1)
	global_store_dwordx4 v[10:11], v[0:3], off sc0 sc1
	s_nop 1
	v_lshl_add_u64 v[0:1], v[8:9], 0, s[2:3]
	s_waitcnt lgkmcnt(0)
	global_store_dwordx4 v[0:1], v[4:7], off sc0 sc1
	ds_read_b128 v[0:3], v12 offset:7280
	ds_read_b128 v[4:7], v12 offset:8320
	s_add_i32 s2, s0, 8
	s_mov_b32 s3, s1
	s_lshl_b64 s[2:3], s[2:3], 10
	v_lshl_add_u64 v[10:11], v[8:9], 0, s[2:3]
	s_add_i32 s2, s0, 9
	s_mov_b32 s3, s1
	s_lshl_b64 s[2:3], s[2:3], 10
	s_waitcnt lgkmcnt(1)
	global_store_dwordx4 v[10:11], v[0:3], off sc0 sc1
	s_nop 1
	v_lshl_add_u64 v[0:1], v[8:9], 0, s[2:3]
	s_waitcnt lgkmcnt(0)
	global_store_dwordx4 v[0:1], v[4:7], off sc0 sc1
	ds_read_b128 v[0:3], v12 offset:9360
	ds_read_b128 v[4:7], v12 offset:10400
	s_add_i32 s2, s0, 10
	s_mov_b32 s3, s1
	s_lshl_b64 s[2:3], s[2:3], 10
	v_lshl_add_u64 v[10:11], v[8:9], 0, s[2:3]
	s_add_i32 s2, s0, 11
	s_mov_b32 s3, s1
	s_lshl_b64 s[2:3], s[2:3], 10
	s_waitcnt lgkmcnt(1)
	global_store_dwordx4 v[10:11], v[0:3], off sc0 sc1
	s_nop 1
	v_lshl_add_u64 v[0:1], v[8:9], 0, s[2:3]
	s_waitcnt lgkmcnt(0)
	global_store_dwordx4 v[0:1], v[4:7], off sc0 sc1
	ds_read_b128 v[0:3], v12 offset:11440
	ds_read_b128 v[4:7], v12 offset:12480
	s_add_i32 s2, s0, 12
	s_mov_b32 s3, s1
	s_lshl_b64 s[2:3], s[2:3], 10
	v_lshl_add_u64 v[10:11], v[8:9], 0, s[2:3]
	s_add_i32 s2, s0, 13
	s_mov_b32 s3, s1
	s_lshl_b64 s[2:3], s[2:3], 10
	s_waitcnt lgkmcnt(1)
	global_store_dwordx4 v[10:11], v[0:3], off sc0 sc1
	s_nop 1
	v_lshl_add_u64 v[0:1], v[8:9], 0, s[2:3]
	s_waitcnt lgkmcnt(0)
	global_store_dwordx4 v[0:1], v[4:7], off sc0 sc1
	ds_read_b128 v[0:3], v12 offset:13520
	ds_read_b128 v[4:7], v12 offset:14560
	s_add_i32 s2, s0, 14
	s_mov_b32 s3, s1
	s_lshl_b64 s[2:3], s[2:3], 10
	s_add_i32 s0, s0, 15
	v_lshl_add_u64 v[10:11], v[8:9], 0, s[2:3]
	s_lshl_b64 s[0:1], s[0:1], 10
	s_waitcnt lgkmcnt(1)
	global_store_dwordx4 v[10:11], v[0:3], off sc0 sc1
	s_nop 1
	v_lshl_add_u64 v[0:1], v[8:9], 0, s[0:1]
	s_waitcnt lgkmcnt(0)
	global_store_dwordx4 v[0:1], v[4:7], off sc0 sc1
	s_endpgm

.LBB2_31:
	v_exp_f32_e32 v49, v40
	v_add_f32_e32 v40, v80, v81
	v_add_f32_e32 v40, v40, v82
	v_add_f32_e32 v40, v40, v83
	v_add_f32_e32 v40, v40, v84
	v_exp_f32_e32 v62, v41
	v_exp_f32_e32 v63, v42
	v_exp_f32_e32 v64, v43
	v_exp_f32_e32 v65, v44
	v_exp_f32_e32 v66, v45
	v_exp_f32_e32 v67, v46
	v_exp_f32_e32 v68, v47
	v_add_f32_e32 v50, v40, v85
	v_cvt_pk_f16_f32 v40, v80, v81
	v_cvt_pk_f16_f32 v41, v82, v83
	v_cvt_pk_f16_f32 v42, v84, v85
	v_cvt_pk_f16_f32 v43, v86, v87
	ds_read_b64_tr_b16 v[44:45], v187 offset:32768
	ds_read_b64_tr_b16 v[46:47], v187 offset:33280
	v_add_f32_e32 v50, v50, v86
	v_add_f32_e32 v54, v50, v87
	ds_read_b64_tr_b16 v[50:51], v187 offset:33792
	ds_read_b64_tr_b16 v[52:53], v187 offset:34304
	s_waitcnt lgkmcnt(2)
	v_mfma_f32_32x32x16_f16 v[0:15], v[40:43], v[44:47], v[0:15]
	ds_read_b64_tr_b16 v[44:45], v187 offset:36864
	ds_read_b64_tr_b16 v[46:47], v187 offset:37376
	v_add_f32_e32 v54, v54, v88
	v_add_f32_e32 v69, v54, v89
	v_cvt_pk_f16_f32 v54, v88, v89
	v_cvt_pk_f16_f32 v55, v90, v91
	v_cvt_pk_f16_f32 v56, v92, v93
	v_cvt_pk_f16_f32 v57, v94, v95
	s_waitcnt lgkmcnt(0)
	v_mfma_f32_32x32x16_f16 v[16:31], v[40:43], v[44:47], v[16:31]
	v_add_f32_e32 v40, v69, v90
	v_add_f32_e32 v40, v40, v91
	v_add_f32_e32 v40, v40, v92
	v_add_f32_e32 v40, v40, v93
	ds_read_b64_tr_b16 v[58:59], v187 offset:37888
	ds_read_b64_tr_b16 v[60:61], v187 offset:38400
	v_add_f32_e32 v40, v40, v94
	v_add_f32_e32 v40, v40, v95
	v_mfma_f32_32x32x16_f16 v[0:15], v[54:57], v[50:53], v[0:15]
	v_add_f32_e32 v40, v40, v32
	v_add_f32_e32 v50, v40, v33
	v_cvt_pk_f16_f32 v40, v32, v33
	v_cvt_pk_f16_f32 v41, v34, v35
	v_cvt_pk_f16_f32 v42, v36, v37
	v_cvt_pk_f16_f32 v43, v38, v39
	ds_read_b64_tr_b16 v[44:45], v187 offset:34816
	ds_read_b64_tr_b16 v[46:47], v187 offset:35328
	s_waitcnt lgkmcnt(2)
	v_mfma_f32_32x32x16_f16 v[16:31], v[54:57], v[58:61], v[16:31]
	v_add_f32_e32 v32, v50, v34
	v_add_f32_e32 v50, v32, v35
	ds_read_b64_tr_b16 v[32:33], v187 offset:35840
	ds_read_b64_tr_b16 v[34:35], v187 offset:36352
	v_add_f32_e32 v36, v50, v36
	v_add_f32_e32 v36, v36, v37
	v_cvt_pk_f16_f32 v50, v49, v62
	v_cvt_pk_f16_f32 v51, v63, v64
	s_waitcnt lgkmcnt(2)
	v_mfma_f32_32x32x16_f16 v[0:15], v[40:43], v[44:47], v[0:15]
	ds_read_b64_tr_b16 v[44:45], v187 offset:38912
	ds_read_b64_tr_b16 v[46:47], v187 offset:39424
	v_cvt_pk_f16_f32 v52, v65, v66
	v_cvt_pk_f16_f32 v53, v67, v68
	ds_read_b64_tr_b16 v[54:55], v187 offset:39936
	ds_read_b64_tr_b16 v[56:57], v187 offset:40448
	v_add_f32_e32 v36, v36, v38
	v_add_f32_e32 v36, v36, v39
	v_add_f32_e32 v36, v36, v49
	s_waitcnt lgkmcnt(2)
	v_mfma_f32_32x32x16_f16 v[16:31], v[40:43], v[44:47], v[16:31]
	v_add_f32_e32 v36, v36, v62
	v_mfma_f32_32x32x16_f16 v[0:15], v[50:53], v[32:35], v[0:15]
	v_add_f32_e32 v32, v36, v63
	v_add_f32_e32 v32, v32, v64
	v_add_f32_e32 v32, v32, v65
	v_add_f32_e32 v32, v32, v66
	v_add_f32_e32 v32, v32, v67
	v_add_f32_e32 v32, v32, v68
	v_add_f32_e32 v32, v188, v32
	s_waitcnt lgkmcnt(0)
	v_mfma_f32_32x32x16_f16 v[16:31], v[50:53], v[54:57], v[16:31]
	v_mov_b32_e32 v33, v32
	s_nop 1
	v_permlane32_swap_b32_e32 v32, v33
	s_and_saveexec_b64 s[2:3], s[0:1]
	v_add_f32_e32 v32, v32, v33
	ds_write_b32 v186, v32 offset:49280
	s_or_b64 exec, exec, s[2:3]
	s_waitcnt lgkmcnt(0)
	ds_read_b128 v[32:35], v48 offset:49280
	ds_read_b128 v[36:39], v48 offset:49312
	s_lshl_b64 s[0:1], s[10:11], 2
	s_add_u32 s0, s6, s0
	s_addc_u32 s1, s7, s1
	s_waitcnt lgkmcnt(1)
	v_rcp_f32_e32 v40, v32
	v_rcp_f32_e32 v41, v33
	s_lshl_b32 s2, s20, 13
	v_rcp_f32_e32 v42, v34
	v_rcp_f32_e32 v43, v35
	s_waitcnt lgkmcnt(0)
	v_rcp_f32_e32 v44, v36
	ds_read_b128 v[32:35], v48 offset:49344
	v_rcp_f32_e32 v45, v37
	v_rcp_f32_e32 v46, v38
	v_rcp_f32_e32 v47, v39
	ds_read_b128 v[36:39], v48 offset:49376
	s_add_i32 s2, s2, 0
	v_lshlrev_b32_e32 v48, 2, v181
	v_add3_u32 v48, s2, v182, v48
	v_mul_f32_e32 v0, v0, v40
	v_mul_f32_e32 v16, v16, v40
	v_add_u32_e32 v40, 0xc800, v48
	ds_write2_b32 v40, v0, v16 offset1:32
	v_mul_f32_e32 v0, v1, v41
	v_mul_f32_e32 v1, v17, v41
	ds_write2_b32 v40, v0, v1 offset0:64 offset1:96
	v_mul_f32_e32 v0, v2, v42
	v_mul_f32_e32 v1, v18, v42
	ds_write2_b32 v40, v0, v1 offset0:128 offset1:160
	v_mul_f32_e32 v0, v3, v43
	v_mul_f32_e32 v1, v19, v43
	s_waitcnt lgkmcnt(4)
	v_rcp_f32_e32 v32, v32
	ds_write2_b32 v40, v0, v1 offset0:192 offset1:224
	v_mul_f32_e32 v0, v4, v44
	v_mul_f32_e32 v1, v20, v44
	v_add_u32_e32 v2, 0xd000, v48
	v_rcp_f32_e32 v33, v33
	ds_write2_b32 v2, v0, v1 offset1:32
	v_mul_f32_e32 v0, v5, v45
	v_mul_f32_e32 v1, v21, v45
	v_rcp_f32_e32 v34, v34
	ds_write2_b32 v2, v0, v1 offset0:64 offset1:96
	v_mul_f32_e32 v0, v6, v46
	v_mul_f32_e32 v1, v22, v46
	v_rcp_f32_e32 v35, v35
	ds_write2_b32 v2, v0, v1 offset0:128 offset1:160
	v_mul_f32_e32 v0, v7, v47
	v_mul_f32_e32 v1, v23, v47
	s_waitcnt lgkmcnt(7)
	v_rcp_f32_e32 v36, v36
	ds_write2_b32 v2, v0, v1 offset0:192 offset1:224
	v_mul_f32_e32 v0, v8, v32
	v_mul_f32_e32 v1, v24, v32
	v_add_u32_e32 v2, 0xd800, v48
	v_rcp_f32_e32 v37, v37
	ds_write2_b32 v2, v0, v1 offset1:32
	v_mul_f32_e32 v0, v9, v33
	v_mul_f32_e32 v1, v25, v33
	v_rcp_f32_e32 v38, v38
	ds_write2_b32 v2, v0, v1 offset0:64 offset1:96
	v_mul_f32_e32 v0, v10, v34
	v_mul_f32_e32 v1, v26, v34
	v_rcp_f32_e32 v39, v39
	ds_write2_b32 v2, v0, v1 offset0:128 offset1:160
	v_mul_f32_e32 v0, v11, v35
	v_mul_f32_e32 v1, v27, v35
	ds_write2_b32 v2, v0, v1 offset0:192 offset1:224
	v_mul_f32_e32 v0, v12, v36
	v_mul_f32_e32 v1, v28, v36
	v_add_u32_e32 v2, 0xe000, v48
	ds_write2_b32 v2, v0, v1 offset1:32
	v_mul_f32_e32 v0, v13, v37
	v_mul_f32_e32 v1, v29, v37
	ds_write2_b32 v2, v0, v1 offset0:64 offset1:96
	v_mul_f32_e32 v0, v14, v38
	v_mul_f32_e32 v1, v30, v38
	ds_write2_b32 v2, v0, v1 offset0:128 offset1:160
	v_mul_f32_e32 v0, v15, v39
	v_mul_f32_e32 v1, v31, v39
	v_and_b32_e32 v8, 0xf0, v185
	ds_write2_b32 v2, v0, v1 offset0:192 offset1:224
	v_add_u32_e32 v14, s2, v8
	s_waitcnt lgkmcnt(0)
	v_lshl_add_u32 v0, v183, 8, v14
	v_or_b32_e32 v15, 4, v183
	s_lshl_b32 s3, s21, 2
	ds_read_b128 v[0:3], v0 offset:51200
	v_lshl_add_u32 v4, v15, 8, v14
	s_add_u32 s0, s0, s3
	ds_read_b128 v[4:7], v4 offset:51200
	s_addc_u32 s1, s1, 0
	v_mov_b32_e32 v9, 0
	v_lshl_add_u64 v[10:11], s[0:1], 0, v[8:9]
	v_lshlrev_b32_e32 v8, 11, v183
	v_lshl_add_u64 v[12:13], v[10:11], 0, v[8:9]
	v_lshlrev_b32_e32 v8, 11, v15
	s_waitcnt lgkmcnt(1)
	global_store_dwordx4 v[12:13], v[0:3], off sc0 sc1
	v_or_b32_e32 v15, 12, v183
	s_nop 0
	v_lshl_add_u64 v[0:1], v[10:11], 0, v[8:9]
	s_waitcnt lgkmcnt(0)
	global_store_dwordx4 v[0:1], v[4:7], off sc0 sc1
	s_nop 1
	v_or_b32_e32 v4, 8, v183
	v_lshl_add_u32 v0, v4, 8, v14
	ds_read_b128 v[0:3], v0 offset:51200
	v_lshlrev_b32_e32 v8, 11, v4
	v_lshl_add_u32 v4, v15, 8, v14
	ds_read_b128 v[4:7], v4 offset:51200
	v_lshl_add_u64 v[12:13], v[10:11], 0, v[8:9]
	v_lshlrev_b32_e32 v8, 11, v15
	s_waitcnt lgkmcnt(1)
	global_store_dwordx4 v[12:13], v[0:3], off sc0 sc1
	v_or_b32_e32 v15, 20, v183
	s_nop 0
	v_lshl_add_u64 v[0:1], v[10:11], 0, v[8:9]
	s_waitcnt lgkmcnt(0)
	global_store_dwordx4 v[0:1], v[4:7], off sc0 sc1
	s_nop 1
	v_or_b32_e32 v4, 16, v183
	v_lshl_add_u32 v0, v4, 8, v14
	ds_read_b128 v[0:3], v0 offset:51200
	v_lshlrev_b32_e32 v8, 11, v4
	v_lshl_add_u32 v4, v15, 8, v14
	ds_read_b128 v[4:7], v4 offset:51200
	v_lshl_add_u64 v[12:13], v[10:11], 0, v[8:9]
	v_lshlrev_b32_e32 v8, 11, v15
	s_waitcnt lgkmcnt(1)
	global_store_dwordx4 v[12:13], v[0:3], off sc0 sc1
	v_or_b32_e32 v15, 28, v183
	s_nop 0
	v_lshl_add_u64 v[0:1], v[10:11], 0, v[8:9]
	s_waitcnt lgkmcnt(0)
	global_store_dwordx4 v[0:1], v[4:7], off sc0 sc1
	s_nop 1
	v_or_b32_e32 v4, 24, v183
	v_lshl_add_u32 v0, v4, 8, v14
	ds_read_b128 v[0:3], v0 offset:51200
	v_lshlrev_b32_e32 v8, 11, v4
	v_lshl_add_u32 v4, v15, 8, v14
	ds_read_b128 v[4:7], v4 offset:51200
	v_lshl_add_u64 v[12:13], v[10:11], 0, v[8:9]
	v_lshlrev_b32_e32 v8, 11, v15
	s_waitcnt lgkmcnt(1)
	global_store_dwordx4 v[12:13], v[0:3], off sc0 sc1
	s_nop 1
	v_lshl_add_u64 v[0:1], v[10:11], 0, v[8:9]
	s_waitcnt lgkmcnt(0)
	global_store_dwordx4 v[0:1], v[4:7], off sc0 sc1
	s_endpgm
